# tile boundaries (MoE gate/up, MoE down, in-proj): the vmcnt(0) drain at the top of the next tile removed; the previous tile's stores and flag atomic retire under the next tile's prologue
# speedup vs baseline: 1.0072x; 1.0072x over previous
; #define LAS __attribute__((address_space(3)))
;     template <class T> __device__ __forceinline__ T* w(size_t off) const { return (T*)(p->ws + off); }
; __device__ __forceinline__ int slot_expert(const int* sm, int slot) {
;     const int l = threadIdx.x & 63;
;     const bool p = (l >= 1 && l < 32) && slot >= ((const LAS int*)sm)[l & 31];
;     return __popcll(__ballot(p)); }
; __device__ __forceinline__ void ph_moe1_mfma(const Ctx& c, int layer, int tile, const int* sm, unsigned char* lds) {
;     ...
;     if (s0 >= sm[32]) return;
;     unsigned* flag = c.w<unsigned>(WS_CTL) + CW_MOEF + (layer * 512 + st) * 16;
;     const int e = slot_expert(sm, s0), base = s0 - sm[e], ce = sm[33 + e];
;     if (base >= ce) { if (c.tid == 0) (void)__hip_atomic_fetch_add(flag, 1u, __ATOMIC_RELAXED, __HIP_MEMORY_SCOPE_AGENT); return; }
.LBB0_141:
	s_or_b64 exec, exec, s[28:29]
	v_cndmask_b32_e64 v2, 0, 1, s[6:7]
	v_cmp_ne_u32_e32 vcc, 0, v2
	s_bcnt1_i32_b64 s7, vcc
	s_lshl_b32 s6, s7, 2
	v_mov_b32_e32 v2, s6
	v_add_u32_e32 v2, 0x8c00, v2
	ds_read2_b32 v[4:5], v2 offset0:16 offset1:49
	s_waitcnt lgkmcnt(0)
	v_sub_u32_e32 v2, s72, v4
	v_cmp_ge_i32_e32 vcc, v2, v5
	s_cbranch_vccnz .LBB0_153
	s_load_dwordx2 s[42:43], s[0:1], 0x130
	v_cmp_eq_u32_e32 vcc, 0, v118
	s_and_saveexec_b64 s[28:29], vcc
	s_cbranch_execz .LBB0_152
	s_lshl_b32 s6, s16, 4
	s_add_i32 s16, s6, s57
	s_ashr_i32 s17, s16, 31
	s_lshl_b64 s[16:17], s[16:17], 2
	s_waitcnt lgkmcnt(0)
	s_add_u32 s6, s42, s16
	s_addc_u32 s16, s43, s17
	s_add_u32 s44, s6, 0x10000
	s_addc_u32 s45, s16, 0
	s_mov_b32 s6, 0x400001
	s_branch .LBB0_145

; #define LAS __attribute__((address_space(3)))
;     template <class T> __device__ __forceinline__ T* w(size_t off) const { return (T*)(p->ws + off); }
; __device__ __forceinline__ int slot_expert(const int* sm, int slot) {
;     const int l = threadIdx.x & 63;
;     const bool p = (l >= 1 && l < 32) && slot >= ((const LAS int*)sm)[l & 31];
;     return __popcll(__ballot(p)); }
; __device__ __forceinline__ void ph_moe2_mfma(const Ctx& c, int layer, int tile, const int* sm, unsigned char* lds) {
;     ...
;     if (s0 >= sm[32]) return;
;     const int e = slot_expert(sm, s0), base = s0 - sm[e], ce = sm[33 + e];
;     if (base >= ce) return;
;     {
;         unsigned* flag = c.w<unsigned>(WS_CTL) + CW_MOEF + (layer * 512 + st) * 16;
;         if (c.tid == 0) {
;             unsigned sp = 0u;
;             while (__hip_atomic_load(flag, __ATOMIC_RELAXED, __HIP_MEMORY_SCOPE_AGENT) < 8u) { __builtin_amdgcn_s_sleep(1); if (++sp > (1u << 22)) break; }
.LBB0_158:
	s_or_b64 exec, exec, s[42:43]
	v_cndmask_b32_e64 v2, 0, 1, s[6:7]
	v_cmp_ne_u32_e32 vcc, 0, v2
	s_bcnt1_i32_b64 s18, vcc
	s_lshl_b32 s6, s18, 2
	v_mov_b32_e32 v2, s6
	v_add_u32_e32 v2, 0x8c00, v2
	ds_read2_b32 v[4:5], v2 offset0:16 offset1:49
	s_load_dwordx2 s[42:43], s[0:1], 0x130
	s_mov_b64 s[6:7], -1
	v_cmp_eq_u32_e64 s[46:47], 0, v118
	s_waitcnt lgkmcnt(0)
	v_sub_u32_e32 v2, s17, v4
	v_cmp_lt_i32_e32 vcc, v2, v5
	s_cbranch_vccnz .LBB0_161
	s_and_b64 s[28:29], s[46:47], exec
	s_cbranch_execz .LBB0_162

;     ...
;     unsigned ao[4];
; #pragma unroll
;     for (int i = 0; i < 4; ++i) ao[i] = arow((tid >> 3) + 32 * i) + (tid & 7) * 8;
;     const int bk = tid >> 4, bnc = tid & 15;
;     constexpr int NRB = B_F32 ? 8 : 4;
;     u32x4 ra0[4], ra1[4]; u32x4 rb0[NRB], rb1[NRB];
;     auto gloadA = [&](int kt, u32x4 (&ra)[4]) __attribute__((always_inline)) {
; #pragma unroll
;         for (int i = 0; i < 4; ++i) ra[i] = *(const u32x4*)(Abase + (ao[i] + kt * 64));
;     };
;     auto gloadB = [&](int kt, u32x4 (&rb)[NRB]) __attribute__((always_inline)) {
;         if (B_F32) {
;             const float* bp = (const float*)Bbase + (boff + (unsigned)((kt * 64 + bk) * ldb));
; #pragma unroll
;             for (int i = 0; i < 4; ++i) {
;                 if (bval) { rb[2 * i] = *(const u32x4*)(bp + (unsigned)(16 * i * ldb)); rb[2 * i + 1] = *(const u32x4*)(bp + (unsigned)(16 * i * ldb) + 4); }
;                 else { rb[2 * i] = (u32x4){0u, 0u, 0u, 0u}; rb[2 * i + 1] = rb[2 * i]; }
;             }
;         } else {
;             const bf16* bp = (const bf16*)Bbase + (boff + (unsigned)((kt * 64 + bk) * ldb));
; #pragma unroll
;             for (int i = 0; i < 4; ++i) rb[i] = bval ? *(const u32x4*)(bp + (unsigned)(16 * i * ldb)) : (u32x4){0u, 0u, 0u, 0u};
;         }
;     };
;     auto lstore = [&](const u32x4 (&ra)[4], const u32x4 (&rb)[NRB]) __attribute__((always_inline)) {
; #pragma unroll
;         for (int i = 0; i < 4; ++i) { const int row = (tid >> 3) + 32 * i, kc = tid & 7;
;             const u32x4 v = (kc & 1) ? (u32x4){ra[i][2], ra[i][3], ra[i][0], ra[i][1]} : ra[i];
;             *(u32x4*)(lds + (kc >> 2) * GA_KH + row * 64 + (kc & 3) * 16) = v; }
; #pragma unroll
; __device__ __forceinline__ void ph_inproj_mfma(const Ctx& c, int layer, int tile, unsigned char* lds) {
;     const int mt = tile / 18, nt = tile % 18;
;     const bf16* HA = c.w<bf16>(WS_HA) + (size_t)mt * 128 * D;
;     f32x4 acc[4][4];
;     const int vc = nt * 128 + (c.tid & 15) * 8;
;     gemm_tile<false, 1>(c.tid, lds, HA, [&](int r) __attribute__((always_inline)) { return (unsigned)(r * D); }, c.w<bf16>(WS_BIN) + (size_t)layer * D * DINV, (unsigned)vc, DINV, true, D, acc);
;     const int lane = c.tid & 63, wid = c.tid >> 6, wr = wid >> 1, wc = wid & 1, fr = lane & 15, fq = lane >> 4;
;     const int n0 = mt * 128, b = n0 / LT, pos0 = n0 % LT;
.LBB0_544:
	s_andn2_b64 vcc, exec, s[0:1]
	s_cbranch_vccnz .LBB0_533
	s_mul_hi_i32 s0, s60, 0x38e38e39
	s_load_dwordx2 s[42:43], s[4:5], 0x130
	s_lshr_b32 s1, s0, 31
	s_ashr_i32 s0, s0, 2
	s_add_i32 s28, s0, s1
	s_mul_i32 s0, s28, 18
	s_ashr_i32 s29, s28, 31
	s_sub_i32 s17, s60, s0
	s_lshl_b64 s[0:1], s[28:29], 18
	s_waitcnt lgkmcnt(0)
	s_add_u32 s0, s42, s0
	s_addc_u32 s1, s43, s1
	s_add_u32 s44, s0, 0x45c6000
	s_addc_u32 s45, s1, 0
	s_lshl_b32 s61, s17, 7
	s_add_u32 s0, s42, s59
	v_lshlrev_b32_e32 v12, 3, v147
	s_addc_u32 s1, s43, s58
	s_add_u32 s46, s0, 0x18095100
	v_lshlrev_b32_e32 v2, 7, v147
	v_and_b32_e32 v4, 56, v12
	s_movk_i32 s0, 0xfc00
	v_and_b32_e32 v155, 15, v147
	v_and_or_b32 v2, v2, s0, v4
	v_lshrrev_b32_e32 v5, 1, v147
	s_mov_b32 s0, 0x3ffffc0
	v_bfe_u32 v157, v147, 4, 2
	v_and_or_b32 v5, v5, s0, v155
	v_bfe_u32 v7, v147, 4, 1
	v_lshlrev_b32_e32 v16, 6, v5
	v_lshlrev_b32_e32 v118, 3, v157
	v_bfe_u32 v5, v147, 2, 2
	v_lshlrev_b32_e32 v9, 2, v7
	v_or3_b32 v5, v9, v5, v118
	v_lshlrev_b32_e32 v9, 1, v147
	v_and_b32_e32 v9, 0x80, v9
	s_movk_i32 s7, 0x120
	v_mad_u32_u24 v5, v5, s7, v9
	v_and_b32_e32 v13, 0x78, v12
	v_add_u32_e32 v4, 0x8000, v2
	v_add_u32_e32 v6, 0x10000, v2
	v_ashrrev_i32_e32 v15, 4, v147
	v_and_or_b32 v119, v12, 24, v5
	v_cmp_eq_u32_e32 vcc, 0, v7
	v_mov_b32_e32 v5, v3
	v_mov_b32_e32 v7, v3
	s_movk_i32 s0, 0x900
	v_or_b32_e32 v14, s61, v13
	v_lshl_add_u64 v[4:5], v[4:5], 1, s[44:45]
	v_lshl_add_u64 v[6:7], v[6:7], 1, s[44:45]
	v_mul_lo_u32 v18, v15, s0
	s_addc_u32 s47, s1, 0
	v_add_u32_e32 v8, 0x18000, v2
	v_mov_b32_e32 v9, v3
	v_add_u32_e32 v6, v14, v18
	v_mov_b32_e32 v7, v3
	v_lshl_add_u64 v[4:5], v[8:9], 1, s[44:45]
	v_lshl_add_u64 v[6:7], v[6:7], 1, s[46:47]
	s_mov_b32 s0, 0x12000
	v_cndmask_b32_e32 v17, v236, v237, vcc
	v_add_co_u32_e32 v4, vcc, s0, v6
	s_mov_b32 s0, 0x24000
	s_nop 0
	v_addc_co_u32_e32 v5, vcc, 0, v7, vcc
	v_add_co_u32_e32 v8, vcc, s0, v6
	s_mov_b32 s0, 0x36000
	s_nop 0
	v_addc_co_u32_e32 v9, vcc, 0, v7, vcc
	v_add_co_u32_e32 v4, vcc, s0, v6
	v_lshl_add_u64 v[10:11], v[2:3], 1, s[44:45]
	s_nop 0
	v_addc_co_u32_e32 v5, vcc, 0, v7, vcc
	v_add_u32_e32 v6, 0x8040, v2
	v_mov_b32_e32 v7, v3
	v_lshl_add_u64 v[6:7], v[6:7], 1, s[44:45]
	v_add_u32_e32 v4, 0x10040, v2
	v_mov_b32_e32 v5, v3
	v_lshl_add_u64 v[4:5], v[4:5], 1, s[44:45]
	v_add_u32_e32 v6, 0x18040, v2
	v_mov_b32_e32 v7, v3
	v_lshl_add_u64 v[6:7], v[6:7], 1, s[44:45]
	v_and_b32_e32 v4, 1, v147
	v_cmp_eq_u32_e64 s[0:1], 0, v4
	v_bfe_i32 v4, v147, 2, 1
	v_and_b32_e32 v4, 0x2040, v4
	v_and_b32_e32 v5, 0xffffffc0, v12
	v_lshl_add_u32 v7, s60, 7, v18
	v_add_u32_e32 v4, v4, v5
	v_lshlrev_b32_e32 v5, 4, v147
	v_mul_lo_u32 v6, v15, s7
	v_or_b32_e32 v7, v7, v13
	s_mul_i32 s7, s28, 0x900
	v_lshlrev_b32_e32 v122, 4, v157
	v_and_b32_e32 v5, 48, v5
	v_lshlrev_b32_e32 v153, 4, v155
	v_subrev_u32_e32 v7, s7, v7
	v_mov_b32_e32 v20, 0
	v_lshrrev_b32_e32 v149, 4, v147
	s_mov_b32 s6, 0
	v_add_u32_e32 v116, 0x48000, v7
	v_add_u32_e32 v120, 0x10080, v2
	v_add_u32_e32 v123, v4, v5
	v_add_u32_e32 v124, v6, v153
	v_add_u32_e32 v125, v16, v122
	v_add_u32_e32 v126, v119, v17
	v_bfe_u32 v120, v147, 2, 2
	v_sub_u32_e32 v120, 0, v120
	v_and_b32_e32 v120, 3, v120
	v_lshlrev_b32_e32 v120, 4, v120
	v_xor_b32_e32 v216, v125, v120
	v_bfe_u32 v120, v147, 4, 2
	v_lshlrev_b32_e32 v120, 3, v120
	v_bfe_u32 v121, v147, 2, 2
	v_add_u32_e32 v120, v120, v121
	v_lshlrev_b32_e32 v120, 8, v120
	v_lshrrev_b32_e32 v68, 6, v147
	v_lshrrev_b32_e32 v214, 4, v147
	v_xor_b32_e32 v68, v68, v214
	v_and_b32_e32 v68, 1, v68
	v_lshlrev_b32_e32 v68, 7, v68
	v_or_b32_e32 v120, v120, v68
	v_and_b32_e32 v68, 3, v147
	v_lshlrev_b32_e32 v68, 3, v68
	v_or_b32_e32 v120, v120, v68
	v_xor_b32_e32 v68, 0, v121
	v_lshl_or_b32 v214, v68, 5, v120
	v_xor_b32_e32 v68, 1, v121
	v_lshl_or_b32 v215, v68, 5, v120
	v_xor_b32_e32 v68, 2, v121
	v_lshl_or_b32 v217, v68, 5, v120
	v_xor_b32_e32 v68, 3, v121
	v_lshl_or_b32 v218, v68, 5, v120
	v_lshrrev_b32_e32 v120, 6, v147
	s_nop 1
	v_readfirstlane_b32 s98, v120
	s_nop 1
	s_lshl_b32 s99, s98, 12
	s_lshl_b32 s98, s98, 11
	s_lshl_b32 s100, s61, 1
	s_add_u32 s46, s46, s100
	s_addc_u32 s47, s47, 0
	v_lshrrev_b32_e32 v120, 6, v147
	v_lshlrev_b32_e32 v120, 5, v120
	v_bfe_u32 v121, v147, 2, 4
	v_add_u32_e32 v120, v120, v121
	v_mul_u32_u24_e32 v120, 0x800, v120
	v_bfe_u32 v121, v147, 4, 2
	v_sub_u32_e32 v121, 0, v121
	v_and_b32_e32 v121, 3, v121
	v_and_b32_e32 v68, 3, v147
	v_xor_b32_e32 v121, v121, v68
	v_lshl_add_u32 v206, v121, 4, v120
	v_add_u32_e32 v207, 64, v206
	v_add_u32_e32 v208, 0x8000, v206
	v_add_u32_e32 v209, 64, v208
	v_lshrrev_b32_e32 v120, 6, v147
	v_lshlrev_b32_e32 v120, 4, v120
	v_bfe_u32 v121, v147, 4, 2
	v_add_u32_e32 v120, v120, v121
	v_mul_u32_u24_e32 v120, 0x1200, v120
	v_bfe_u32 v68, v147, 1, 3
	v_xor_b32_e32 v68, v68, v121
	v_lshlrev_b32_e32 v68, 1, v68
	v_and_b32_e32 v121, 1, v147
	v_or_b32_e32 v68, v68, v121
	v_lshl_add_u32 v210, v68, 4, v120
	v_add_u32_e32 v211, 0x4800, v210
	v_xor_b32_e32 v68, 8, v68
	v_lshl_add_u32 v212, v68, 4, v120
	v_add_u32_e32 v212, 0x9000, v212
	v_add_u32_e32 v213, 0x4800, v212
	s_cmp_lg_u32 s101, 0
	s_cbranch_scc1 .Lip_havepf
	s_barrier
	s_add_u32 m0, s98, 0x0
	s_nop 0
	global_load_lds_dwordx4 v206, s[44:45]
	s_add_u32 m0, s98, 0x2040
	s_nop 0
	global_load_lds_dwordx4 v207, s[44:45]
	s_add_u32 m0, s98, 0x400
	s_nop 0
	global_load_lds_dwordx4 v208, s[44:45]
	s_add_u32 m0, s98, 0x2440
	s_nop 0
	global_load_lds_dwordx4 v209, s[44:45]
	s_add_u32 m0, s99, 0x4080
	s_nop 0
	global_load_lds_dwordx4 v210, s[46:47]
	s_add_u32 m0, s99, 0x4480
	s_nop 0
	global_load_lds_dwordx4 v211, s[46:47]
	s_add_u32 m0, s99, 0x4880
	s_nop 0
	global_load_lds_dwordx4 v212, s[46:47]
	s_add_u32 m0, s99, 0x4c80
	s_nop 0
	global_load_lds_dwordx4 v213, s[46:47]
